# v3 + next work-queue index fetched early (returning atomic issued four tiles before the end of the GQA tile loop, dequeue only waits for it)
# baseline (speedup 1.0000x reference)
_Z10hybrid_fwd4Args:
	s_mov_b64 s[84:85], s[0:1]
	s_mov_b32 s4, 0
	v_writelane_b32 v255, s4, 62
	v_writelane_b32 v252, s2, 0
	s_load_dwordx4 s[0:3], s[84:85], 0x100
	v_readfirstlane_b32 s22, v0
	s_and_b32 s4, s22, 0xffffffc0
	v_mbcnt_lo_u32_b32 v1, -1, 0
	v_mbcnt_hi_u32_b32 v195, -1, v1
	s_waitcnt lgkmcnt(0)
	v_writelane_b32 v252, s0, 1
	v_add_u32_e32 v1, s4, v195
	v_cmp_gt_i32_e32 vcc, 64, v1
	v_writelane_b32 v252, s1, 2
	v_writelane_b32 v252, s2, 3
	v_writelane_b32 v252, s3, 4
	s_load_dword s0, s[84:85], 0x120
	s_waitcnt lgkmcnt(0)
	v_writelane_b32 v252, s0, 5
	s_add_u32 s0, s84, 0x120
	v_writelane_b32 v252, s4, 6
	s_addc_u32 s1, s85, 0
	v_writelane_b32 v252, s0, 7
	s_nop 1
	v_writelane_b32 v252, s1, 8
	s_and_saveexec_b64 s[0:1], vcc
	v_lshl_add_u32 v1, v1, 2, 0
	v_add_u32_e32 v1, 0x20000, v1
	v_mov_b32_e32 v2, 0
	ds_write_b32 v1, v2
	s_or_b64 exec, exec, s[0:1]
	s_load_dwordx4 s[4:7], s[84:85], 0x110
	s_waitcnt lgkmcnt(0)
	s_barrier
	s_getreg_b32 s2, hwreg(HW_REG_XCC_ID, 0, 4)
	s_mov_b64 s[0:1], s[4:5]
	v_writelane_b32 v252, s0, 9
	s_nop 1
	v_writelane_b32 v252, s1, 10
	v_writelane_b32 v252, s2, 11
	v_writelane_b32 v252, s3, 12
	s_mul_i32 s0, s6, 0xd80
	s_load_dwordx4 s[4:7], s[84:85], 0x100
	s_ashr_i32 s1, s0, 31
	s_lshl_b64 s[0:1], s[0:1], 2
	s_waitcnt lgkmcnt(0)
	s_add_u32 s0, s6, s0
	s_addc_u32 s1, s7, s1
	s_add_u32 s0, s0, 0x4000
	s_addc_u32 s1, s1, 0
	v_writelane_b32 v252, s0, 13
	s_and_b32 s23, s2, 15
	v_cmp_eq_u32_e64 s[2:3], 0, v0
	v_writelane_b32 v252, s1, 14
	s_mov_b64 s[0:1], exec
	v_writelane_b32 v252, s2, 15
	s_nop 1
	v_writelane_b32 v252, s3, 16
	s_and_b64 s[2:3], s[0:1], s[2:3]
	s_mov_b64 exec, s[2:3]
	s_cbranch_execz .LBB0_5
	s_mov_b64 s[2:3], exec
	v_mbcnt_lo_u32_b32 v0, s2, 0
	v_mbcnt_hi_u32_b32 v0, s3, v0
	v_cmp_eq_u32_e32 vcc, 0, v0
	s_and_b64 s[4:5], exec, vcc
	s_mov_b64 exec, s[4:5]
	s_cbranch_execz .LBB0_5
	s_bcnt1_i32_b64 s2, s[2:3]
	s_lshl_b32 s4, s23, 8
	v_mov_b32_e32 v1, s2
	v_readlane_b32 s2, v252, 13
	v_mov_b32_e32 v0, s4
	v_readlane_b32 s3, v252, 14
	s_nop 4
	global_atomic_add v0, v1, s[2:3] offset:1024

.LBB0_654:
	v_cmp_eq_u32_e32 vcc, 0, v198
	s_barrier
	s_and_saveexec_b64 s[0:1], vcc
	s_cbranch_execz .LBB0_658
	s_mov_b64 s[6:7], exec
	s_waitcnt vmcnt(7)
	v_mbcnt_lo_u32_b32 v0, s6, 0
	v_mbcnt_hi_u32_b32 v0, s7, v0
	v_cmp_eq_u32_e32 vcc, 0, v0
	s_and_saveexec_b64 s[4:5], vcc
	s_cbranch_execz .LBB0_657
	v_readlane_b32 s2, v255, 62
	s_cmp_eq_u32 s2, 0
	s_cbranch_scc1 .Ldq_nopf
	s_mov_b32 s2, 0
	v_writelane_b32 v255, s2, 62
	s_waitcnt vmcnt(0)
	v_mov_b32_e32 v1, v246
	s_branch .LBB0_657
.Ldq_nopf:
	s_bcnt1_i32_b64 s2, s[6:7]
	v_mov_b32_e32 v1, s2
	v_readlane_b32 s2, v254, 60
	v_readlane_b32 s3, v254, 61
	s_nop 4
	global_atomic_add v1, v193, v1, s[2:3] sc0

.Lfa_loop:
	s_cmp_lg_u32 s29, 64
	s_cbranch_scc1 .Lfa_nopf
	v_readlane_b32 s10, v252, 6
	s_cmp_lg_u32 s10, 0
	s_cbranch_scc1 .Lfa_nopf
	s_mov_b64 s[14:15], exec
	s_mov_b64 exec, 1
	v_readlane_b32 s10, v254, 60
	v_readlane_b32 s11, v254, 61
	v_mov_b32_e32 v246, 1
	s_nop 4
	global_atomic_add v246, v193, v246, s[10:11] sc0
	s_mov_b64 exec, s[14:15]
	s_mov_b32 s10, 1
	v_writelane_b32 v255, s10, 62
